# edge kernels: the 424 seven-tile waves are one wave in each of 424 workgroups (rotating wave slot) instead of all four waves of the first 106 workgroups
# speedup vs baseline: 1.0005x; 1.0005x over previous
.LBB3_4:
	s_or_b64 exec, exec, s[6:7]
	s_lshr_b32 s86, s2, 3
	s_lshr_b32 s87, s86, 5
	s_add_u32 s86, s86, s87
	v_subrev_u32_e32 v56, s86, v32
	v_and_b32_e32 v56, 3, v56
	v_lshl_or_b32 v56, v56, 10, s2
	v_min_i32_e32 v32, 0x61a7, v56
	v_lshl_or_b32 v52, v32, 5, v62
	v_ashrrev_i32_e32 v53, 31, v52
	v_lshl_add_u64 v[58:59], v[52:53], 4, s[8:9]
	v_max_i32_e32 v32, 1, v52
	v_mov_b32_e32 v33, 0
	v_lshl_add_u64 v[60:61], v[32:33], 4, s[8:9]
	global_load_dwordx4 v[32:35], v[58:59], off
	global_load_dword v63, v[58:59], off offset:24
	global_load_dword v53, v[60:61], off offset:-8
	s_load_dword s6, s[0:1], 0x40
	s_waitcnt vmcnt(13)
	ds_write_b128 v30, v[14:17] offset:12800
	s_waitcnt vmcnt(12)
	ds_write_b128 v30, v[22:25] offset:16896
	s_waitcnt vmcnt(10)
	ds_write_b128 v30, v[48:51] offset:20992
	s_waitcnt vmcnt(9)
	v_cvt_f16_f32_e32 v14, v40
	v_cvt_f16_f32_e32 v15, v43
	v_cvt_pk_f16_f32 v17, v41, v42
	s_waitcnt vmcnt(8)
	v_cvt_f16_f32_e32 v23, v47
	v_pack_b32_f16 v16, v14, v17
	v_alignbit_b32 v17, v15, v17, 16
	v_cvt_f16_f32_e32 v15, v44
	v_cvt_pk_f16_f32 v24, v45, v46
	v_lshlrev_b32_e32 v14, 3, v0
	v_alignbit_b32 v23, v23, v24, 16
	v_pack_b32_f16 v22, v15, v24
	s_waitcnt vmcnt(7)
	v_cvt_f16_f32_e32 v15, v18
	ds_write2st64_b64 v14, v[16:17], v[22:23] offset1:4
	v_cvt_pk_f16_f32 v17, v19, v20
	v_cvt_f16_f32_e32 v18, v21
	v_pack_b32_f16 v16, v15, v17
	s_waitcnt vmcnt(6)
	v_cvt_f16_f32_e32 v15, v26
	v_cvt_f16_f32_e32 v19, v29
	s_waitcnt vmcnt(5)
	v_cvt_f16_f32_e32 v6, v6
	v_cvt_pk_f16_f32 v7, v7, v8
	v_cvt_f16_f32_e32 v8, v9
	s_waitcnt vmcnt(4)
	v_cvt_f16_f32_e32 v9, v10
	v_cvt_f16_f32_e32 v10, v13
	v_cvt_pk_f16_f32 v20, v27, v28
	v_cvt_pk_f16_f32 v11, v11, v12
	v_alignbit_b32 v17, v18, v17, 16
	v_pack_b32_f16 v18, v15, v20
	v_alignbit_b32 v19, v19, v20, 16
	v_pack_b32_f16 v6, v6, v7
	v_alignbit_b32 v7, v8, v7, 16
	v_pack_b32_f16 v8, v9, v11
	v_alignbit_b32 v9, v10, v11, 16
	ds_write_b128 v30, v[36:39] offset:25088
	ds_write2st64_b64 v14, v[16:17], v[18:19] offset0:8 offset1:12
	ds_write2st64_b64 v14, v[6:7], v[8:9] offset0:16 offset1:20
	s_and_saveexec_b64 s[2:3], vcc
	s_cbranch_execnz .LBB3_74
	s_or_b64 exec, exec, s[2:3]
	s_and_saveexec_b64 s[2:3], vcc
	s_cbranch_execnz .LBB3_75

.LBB4_4:
	s_or_b64 exec, exec, s[6:7]
	s_lshr_b32 s86, s2, 3
	s_lshr_b32 s87, s86, 5
	s_add_u32 s86, s86, s87
	v_subrev_u32_e32 v64, s86, v48
	v_and_b32_e32 v64, 3, v64
	v_lshl_or_b32 v64, v64, 10, s2
	v_min_i32_e32 v48, 0x61a7, v64
	v_lshl_or_b32 v54, v48, 5, v66
	v_ashrrev_i32_e32 v55, 31, v54
	v_lshl_add_u64 v[56:57], v[54:55], 4, s[8:9]
	v_max_i32_e32 v48, 1, v54
	v_mov_b32_e32 v49, 0
	v_lshl_add_u64 v[58:59], v[48:49], 4, s[8:9]
	global_load_dwordx4 v[48:51], v[56:57], off
	global_load_dword v80, v[56:57], off offset:24
	global_load_dword v55, v[58:59], off offset:-8
	s_load_dword s10, s[0:1], 0x48
	s_waitcnt vmcnt(13)
	ds_write_b128 v46, v[14:17] offset:12800
	s_waitcnt vmcnt(12)
	ds_write_b128 v46, v[22:25] offset:16896
	s_waitcnt vmcnt(10)
	ds_write_b128 v46, v[42:45] offset:20992
	s_waitcnt vmcnt(9)
	v_cvt_f16_f32_e32 v14, v34
	v_cvt_f16_f32_e32 v15, v37
	v_cvt_pk_f16_f32 v17, v35, v36
	s_waitcnt vmcnt(8)
	v_cvt_f16_f32_e32 v23, v41
	v_pack_b32_f16 v16, v14, v17
	v_alignbit_b32 v17, v15, v17, 16
	v_cvt_f16_f32_e32 v15, v38
	v_cvt_pk_f16_f32 v24, v39, v40
	v_lshlrev_b32_e32 v14, 3, v0
	v_alignbit_b32 v23, v23, v24, 16
	v_pack_b32_f16 v22, v15, v24
	s_waitcnt vmcnt(7)
	v_cvt_f16_f32_e32 v15, v18
	ds_write2st64_b64 v14, v[16:17], v[22:23] offset1:4
	v_cvt_pk_f16_f32 v17, v19, v20
	v_cvt_f16_f32_e32 v18, v21
	v_pack_b32_f16 v16, v15, v17
	s_waitcnt vmcnt(6)
	v_cvt_f16_f32_e32 v15, v26
	v_cvt_f16_f32_e32 v19, v29
	s_waitcnt vmcnt(5)
	v_cvt_f16_f32_e32 v6, v6
	v_cvt_pk_f16_f32 v7, v7, v8
	v_cvt_f16_f32_e32 v8, v9
	s_waitcnt vmcnt(4)
	v_cvt_f16_f32_e32 v9, v10
	v_cvt_f16_f32_e32 v10, v13
	v_cvt_pk_f16_f32 v20, v27, v28
	v_cvt_pk_f16_f32 v11, v11, v12
	v_alignbit_b32 v17, v18, v17, 16
	v_pack_b32_f16 v18, v15, v20
	v_alignbit_b32 v19, v19, v20, 16
	v_pack_b32_f16 v6, v6, v7
	v_alignbit_b32 v7, v8, v7, 16
	v_pack_b32_f16 v8, v9, v11
	v_alignbit_b32 v9, v10, v11, 16
	ds_write_b128 v46, v[30:33] offset:25088
	ds_write2st64_b64 v14, v[16:17], v[18:19] offset0:8 offset1:12
	ds_write2st64_b64 v14, v[6:7], v[8:9] offset0:16 offset1:20
	s_and_saveexec_b64 s[2:3], vcc
	s_cbranch_execnz .LBB4_74
	s_or_b64 exec, exec, s[2:3]
	s_and_saveexec_b64 s[2:3], vcc
	s_cbranch_execnz .LBB4_75
